# MoE gate/up GEMM: leading wave group's alignment barrier moved to the tail of its epilogue (as in the MoE-down GEMM)
# speedup vs baseline: 1.0102x; 1.0014x over previous
; __device__ __forceinline__ unsigned cvt4_fp8(float a, float b, float c, float d) { int w = 0; w = __builtin_amdgcn_cvt_pk_fp8_f32(a, b, w, false); w = __builtin_amdgcn_cvt_pk_fp8_f32(c, d, w, true); return (unsigned)w; }
; __device__ __forceinline__ float sig1702_(float x) { return __builtin_amdgcn_rcpf(1.0f + __builtin_amdgcn_exp2f(x * -2.4554669f)); }
; #define PG8_BAR __builtin_amdgcn_s_barrier()
; template <class Epi, class Sched, bool GATHER, bool ALIGN_EPI, bool SP2, bool FP8>
; __device__ __forceinline__ void gemm_phase(LAS unsigned char* lds, const Gemm g, const Sched& S, const Epi& E) {
;     ...
;         if constexpr (ALIGN_EPI) { if (wr == 0) PG8_BAR; }
;         {
;             asm volatile("s_nop 15\n\ts_nop 3" : "+v"(acc[0][0][0][0]), "+v"(acc[0][0][0][1]), "+v"(acc[0][0][1][0]), "+v"(acc[0][0][1][1]), "+v"(acc[0][0][2][0]), "+v"(acc[0][0][2][1]), "+v"(acc[0][0][3][0]), "+v"(acc[0][0][3][1]));
;     __device__ __forceinline__ void operator()(const f32x4 (&acc)[2][2][4][2], const pg8::Unit& u, const Pre& pre, int wr, int wc, int fr, int fq) const {
;         const int e = u.e, cn = u.pn - e * 16, col = cn * 128 + wc * 32 + 8 * fq, ce = cnt[e];
;         const f32x4 g0 = pre.g0, g1 = pre.g1, u0 = pre.u0, u1 = pre.u1;
;         float rsv[8];
; #pragma unroll
;         for (int i = 0; i < 8; ++i) { const int p = u.r0 + (i >> 2) * 128 + wr * 64 + (i & 3) * 16 + fr; rsv[i] = list_rs[e * LIST_STRIDE + (p < ce ? p : 0)]; }
; #pragma unroll
;         for (int ai = 0; ai < 2; ++ai)
; #pragma unroll
;             for (int m = 0; m < 4; ++m) { const int rit = ai * 128 + wr * 64 + m * 16 + fr, p = u.r0 + rit; const float rs = (p < ce) ? rsv[ai * 4 + m] * 0.015625f : 0.f;
;                 f32x4 gt0 = acc[ai][0][m][0] * rs + g0, gt1 = acc[ai][0][m][1] * rs + g1, up0 = acc[ai][1][m][0] * rs + u0, up1 = acc[ai][1][m][1] * rs + u1;
;                 float o[8];
; #pragma unroll
;                 for (int j = 0; j < 4; ++j) { float gv = fminf(gt0[j], 7.0f), uv = fminf(fmaxf(up0[j], -7.0f), 7.0f); o[j] = (uv + 1.0f) * (gv * sig1702_(gv));
;                     gv = fminf(gt1[j], 7.0f); uv = fminf(fmaxf(up1[j], -7.0f), 7.0f); o[4 + j] = (uv + 1.0f) * (gv * sig1702_(gv)); }
;                 u32x2 w; w.x = cvt4_fp8(o[0], o[1], o[2], o[3]); w.y = cvt4_fp8(o[4], o[5], o[6], o[7]);
;                 *(u32x2*)(ACT + (size_t)(u.pm * 256 + rit) * DFF + col) = w; }
.LBB0_934:
.LBB0_936:
	s_nop 15
	s_nop 3
	s_lshl_b32 s3, s33, 2
	s_add_i32 s3, s3, 0
	s_add_i32 s3, s3, 0x27e00
	v_mov_b32_e32 v6, v0
	v_mov_b32_e32 v2, s3
	ds_read_b32 v4, v2
	v_readfirstlane_b32 s2, v6
	s_ashr_i32 s3, s2, 2
	s_andn2_b32 s3, s3, 63
	v_and_or_b32 v5, v6, 15, s3
	v_add_u32_e32 v2, s50, v5
	s_waitcnt lgkmcnt(0)
	v_cmp_lt_i32_e64 s[8:9], v2, v4
	s_lshl_b32 s18, s33, 14
	v_add_u32_e32 v8, 0x80, v5
	v_cndmask_b32_e64 v2, 0, v2, s[8:9]
	v_add_u32_e32 v2, s18, v2
	v_ashrrev_i32_e32 v3, 31, v2
	v_lshl_add_u64 v[2:3], v[2:3], 2, s[28:29]
	v_mov_b32_e32 v183, v240
	v_add_u32_e32 v11, s50, v8
	s_lshl_b32 s3, s81, 7
	s_lshl_b32 s4, s33, 11
	s_lshr_b32 s2, s2, 1
	v_or_b32_e32 v186, 16, v5
	v_add_u32_e32 v12, 16, v11
	v_lshrrev_b32_e32 v2, 1, v6
	s_sub_i32 s3, s3, s4
	s_and_b32 s2, s2, 0x60
	v_or_b32_e32 v187, 32, v5
	v_or_b32_e32 v10, 48, v5
	v_add_u32_e32 v6, s50, v186
	v_add_u32_e32 v13, 32, v11
	v_cmp_lt_i32_e64 s[10:11], v12, v4
	s_or_b32 s2, s2, s3
	v_add_u32_e32 v7, s50, v187
	v_add_u32_e32 v9, s50, v10
	v_add_u32_e32 v14, 48, v11
	v_cmp_lt_i32_e64 s[6:7], v6, v4
	v_cndmask_b32_e64 v15, 0, v12, s[10:11]
	v_cmp_lt_i32_e64 s[10:11], v13, v4
	v_and_or_b32 v2, v2, 24, s2
	v_cndmask_b32_e64 v6, 0, v6, s[6:7]
	v_cmp_lt_i32_e64 s[4:5], v7, v4
	v_cmp_lt_i32_e64 s[2:3], v9, v4
	v_cmp_lt_i32_e32 vcc, v11, v4
	v_cndmask_b32_e64 v13, 0, v13, s[10:11]
	v_cmp_lt_i32_e64 s[10:11], v14, v4
	v_cndmask_b32_e64 v7, 0, v7, s[4:5]
	v_cndmask_b32_e64 v9, 0, v9, s[2:3]
	v_cndmask_b32_e32 v11, 0, v11, vcc
	v_cndmask_b32_e64 v17, 0, v14, s[10:11]
	v_add_u32_e32 v6, s18, v6
	v_add_u32_e32 v12, s18, v7
	v_add_u32_e32 v14, s18, v9
	v_add_u32_e32 v16, s18, v11
	v_add_u32_e32 v166, s18, v15
	v_add_u32_e32 v168, s18, v13
	v_add_u32_e32 v184, s18, v17
	v_ashrrev_i32_e32 v7, 31, v6
	v_ashrrev_i32_e32 v13, 31, v12
	v_ashrrev_i32_e32 v15, 31, v14
	v_ashrrev_i32_e32 v17, 31, v16
	v_ashrrev_i32_e32 v167, 31, v166
	v_ashrrev_i32_e32 v169, 31, v168
	v_ashrrev_i32_e32 v185, 31, v184
	v_lshl_add_u64 v[6:7], v[6:7], 2, s[28:29]
	v_lshl_add_u64 v[12:13], v[12:13], 2, s[28:29]
	v_lshl_add_u64 v[14:15], v[14:15], 2, s[28:29]
	v_lshl_add_u64 v[16:17], v[16:17], 2, s[28:29]
	v_lshl_add_u64 v[166:167], v[166:167], 2, s[28:29]
	v_lshl_add_u64 v[168:169], v[168:169], 2, s[28:29]
	v_lshl_add_u64 v[184:185], v[184:185], 2, s[28:29]
	v_mov_b32_e32 v188, v241
	v_mov_b32_e32 v189, v242
	v_mov_b32_e32 v190, v243
	v_mov_b32_e32 v11, v246
	v_mov_b32_e32 v9, v247
	s_nop 0
	global_load_dword v7, v[168:169], off
	global_load_dword v6, v[184:185], off
	v_ashrrev_i32_e32 v3, 31, v2
	s_waitcnt vmcnt(7)
	v_mul_f32_e32 v12, 0x3c800000, v183
	v_cndmask_b32_e64 v12, 0, v12, s[8:9]
	v_fma_f32 v13, v158, v12, v26
	v_min_f32_e32 v13, 0x40e00000, v13
	v_fma_f32 v16, v146, v12, v18
	v_mul_f32_e32 v146, 0xc01d265f, v13
	v_exp_f32_e32 v146, v146
	v_fma_f32 v14, v150, v12, v30
	v_fma_f32 v17, v159, v12, v27
	v_med3_f32 v14, v14, s73, v178
	v_add_f32_e32 v146, 1.0, v146
	v_rcp_f32_e32 v146, v146
	v_min_f32_e32 v17, 0x40e00000, v17
	v_fma_f32 v15, v154, v12, v22
	v_add_f32_e32 v14, 1.0, v14
	v_mul_f32_e32 v154, 0xc01d265f, v17
	v_mul_f32_e32 v13, v13, v146
	v_min_f32_e32 v15, 0x40e00000, v15
	v_mul_f32_e32 v13, v14, v13
	v_exp_f32_e32 v14, v154
	v_mul_f32_e32 v150, 0xc01d265f, v15
	v_exp_f32_e32 v150, v150
	v_med3_f32 v16, v16, s73, v178
	v_add_f32_e32 v14, 1.0, v14
	v_rcp_f32_e32 v14, v14
	v_add_f32_e32 v150, 1.0, v150
	v_rcp_f32_e32 v150, v150
	v_add_f32_e32 v16, 1.0, v16
	v_mul_f32_e32 v14, v17, v14
	v_fma_f32 v17, v155, v12, v23
	v_min_f32_e32 v17, 0x40e00000, v17
	v_mul_f32_e32 v15, v15, v150
	v_mul_f32_e32 v146, 0xc01d265f, v17
	v_mul_f32_e32 v15, v16, v15
	v_fma_f32 v16, v151, v12, v31
	v_exp_f32_e32 v146, v146
	v_med3_f32 v16, v16, s73, v178
	v_add_f32_e32 v16, 1.0, v16
	v_mul_f32_e32 v14, v16, v14
	v_fma_f32 v16, v147, v12, v19
	v_fma_f32 v147, v160, v12, v28
	v_add_f32_e32 v146, 1.0, v146
	v_min_f32_e32 v147, 0x40e00000, v147
	v_rcp_f32_e32 v146, v146
	v_mul_f32_e32 v150, 0xc01d265f, v147
	v_exp_f32_e32 v150, v150
	v_med3_f32 v16, v16, s73, v178
	v_add_f32_e32 v16, 1.0, v16
	v_mul_f32_e32 v17, v17, v146
	v_mul_f32_e32 v16, v16, v17
	v_add_f32_e32 v17, 1.0, v150
	v_rcp_f32_e32 v17, v17
	v_fma_f32 v146, v152, v12, v32
	v_med3_f32 v146, v146, s73, v178
	v_add_f32_e32 v146, 1.0, v146
	v_mul_f32_e32 v17, v147, v17
	v_fma_f32 v147, v156, v12, v24
	v_min_f32_e32 v147, 0x40e00000, v147
	v_mul_f32_e32 v150, 0xc01d265f, v147
	v_exp_f32_e32 v150, v150
	v_mul_f32_e32 v17, v146, v17
	v_fma_f32 v146, v148, v12, v20
	v_med3_f32 v146, v146, s73, v178
	v_add_f32_e32 v148, 1.0, v150
	v_fma_f32 v150, v161, v12, v29
	v_min_f32_e32 v150, 0x40e00000, v150
	v_rcp_f32_e32 v148, v148
	v_mul_f32_e32 v151, 0xc01d265f, v150
	v_exp_f32_e32 v151, v151
	v_add_f32_e32 v146, 1.0, v146
	v_mul_f32_e32 v147, v147, v148
	v_mul_f32_e32 v146, v146, v147
	v_add_f32_e32 v147, 1.0, v151
	v_rcp_f32_e32 v147, v147
	v_fma_f32 v148, v153, v12, v33
	v_med3_f32 v148, v148, s73, v178
	v_add_f32_e32 v148, 1.0, v148
	v_mul_f32_e32 v147, v150, v147
	v_mul_f32_e32 v147, v148, v147
	v_fma_f32 v148, v157, v12, v25
	v_min_f32_e32 v148, 0x40e00000, v148
	v_mul_f32_e32 v150, 0xc01d265f, v148
	v_exp_f32_e32 v150, v150
	v_fma_f32 v12, v149, v12, v21
	v_med3_f32 v12, v12, s73, v178
	v_add_f32_e32 v149, 1.0, v12
	v_add_f32_e32 v12, 1.0, v150
	v_rcp_f32_e32 v150, v12
	v_mov_b32_e32 v12, 0
	v_cvt_pk_fp8_f32 v12, v13, v14
	v_mov_b32_e32 v13, 0
	v_cvt_pk_fp8_f32 v13, v15, v16
	s_waitcnt vmcnt(6)
; __device__ __forceinline__ unsigned cvt4_fp8(float a, float b, float c, float d) { int w = 0; w = __builtin_amdgcn_cvt_pk_fp8_f32(a, b, w, false); w = __builtin_amdgcn_cvt_pk_fp8_f32(c, d, w, true); return (unsigned)w; }
; __device__ __forceinline__ float sig1702_(float x) { return __builtin_amdgcn_rcpf(1.0f + __builtin_amdgcn_exp2f(x * -2.4554669f)); }
;     __device__ __forceinline__ void operator()(const f32x4 (&acc)[2][2][4][2], const pg8::Unit& u, const Pre& pre, int wr, int wc, int fr, int fq) const {
;     ...
;         for (int i = 0; i < 8; ++i) { const int p = u.r0 + (i >> 2) * 128 + wr * 64 + (i & 3) * 16 + fr; rsv[i] = list_rs[e * LIST_STRIDE + (p < ce ? p : 0)]; }
; #pragma unroll
;         for (int ai = 0; ai < 2; ++ai)
; #pragma unroll
;             for (int m = 0; m < 4; ++m) { const int rit = ai * 128 + wr * 64 + m * 16 + fr, p = u.r0 + rit; const float rs = (p < ce) ? rsv[ai * 4 + m] * 0.015625f : 0.f;
;                 f32x4 gt0 = acc[ai][0][m][0] * rs + g0, gt1 = acc[ai][0][m][1] * rs + g1, up0 = acc[ai][1][m][0] * rs + u0, up1 = acc[ai][1][m][1] * rs + u1;
;                 float o[8];
; #pragma unroll
;                 for (int j = 0; j < 4; ++j) { float gv = fminf(gt0[j], 7.0f), uv = fminf(fmaxf(up0[j], -7.0f), 7.0f); o[j] = (uv + 1.0f) * (gv * sig1702_(gv));
;                     gv = fminf(gt1[j], 7.0f); uv = fminf(fmaxf(up1[j], -7.0f), 7.0f); o[4 + j] = (uv + 1.0f) * (gv * sig1702_(gv)); }
;                 u32x2 w; w.x = cvt4_fp8(o[0], o[1], o[2], o[3]); w.y = cvt4_fp8(o[4], o[5], o[6], o[7]);
;                 *(u32x2*)(ACT + (size_t)(u.pm * 256 + rit) * DFF + col) = w; }
	v_mul_f32_e32 v16, 0x3c800000, v188
	v_mul_f32_e32 v14, v148, v150
	v_cndmask_b32_e64 v16, 0, v16, s[6:7]
	v_mul_f32_e32 v14, v149, v14
	v_cvt_pk_fp8_f32 v12, v17, v147 op_sel:[0,0,1]
	s_lshl_b32 s8, s79, 8
	v_fma_f32 v17, v142, v16, v26
	v_cvt_pk_fp8_f32 v13, v146, v14 op_sel:[0,0,1]
	v_add_u32_e32 v14, s8, v5
	v_min_f32_e32 v17, 0x40e00000, v17
	v_ashrrev_i32_e32 v15, 31, v14
	v_mul_f32_e32 v142, 0xc01d265f, v17
	v_lshlrev_b64 v[14:15], 11, v[14:15]
	v_exp_f32_e32 v142, v142
	v_lshl_add_u64 v[14:15], s[26:27], 0, v[14:15]
	v_lshl_add_u64 v[14:15], v[14:15], 0, v[2:3]
	global_store_dwordx2 v[14:15], v[12:13], off
	v_fma_f32 v14, v138, v16, v22
	v_add_f32_e32 v12, 1.0, v142
	v_min_f32_e32 v14, 0x40e00000, v14
	v_rcp_f32_e32 v12, v12
	v_mul_f32_e32 v15, 0xc01d265f, v14
	v_exp_f32_e32 v15, v15
	v_fma_f32 v13, v134, v16, v30
	v_med3_f32 v13, v13, s73, v178
	v_mul_f32_e32 v12, v17, v12
	v_fma_f32 v17, v143, v16, v27
	v_add_f32_e32 v13, 1.0, v13
	v_add_f32_e32 v15, 1.0, v15
	v_min_f32_e32 v17, 0x40e00000, v17
	v_mul_f32_e32 v13, v13, v12
	v_fma_f32 v12, v130, v16, v18
	v_rcp_f32_e32 v15, v15
	v_mul_f32_e32 v130, 0xc01d265f, v17
	v_exp_f32_e32 v130, v130
	v_med3_f32 v12, v12, s73, v178
	v_add_f32_e32 v12, 1.0, v12
	v_mul_f32_e32 v14, v14, v15
	v_mul_f32_e32 v14, v12, v14
	v_add_f32_e32 v12, 1.0, v130
	v_rcp_f32_e32 v12, v12
	v_fma_f32 v15, v135, v16, v31
	v_med3_f32 v15, v15, s73, v178
	v_add_f32_e32 v15, 1.0, v15
	v_mul_f32_e32 v12, v17, v12
	v_fma_f32 v17, v139, v16, v23
	v_min_f32_e32 v17, 0x40e00000, v17
	v_mul_f32_e32 v130, 0xc01d265f, v17
	v_exp_f32_e32 v130, v130
	v_mul_f32_e32 v15, v15, v12
	v_fma_f32 v12, v131, v16, v19
	v_fma_f32 v131, v144, v16, v28
	v_add_f32_e32 v130, 1.0, v130
	v_min_f32_e32 v131, 0x40e00000, v131
	v_rcp_f32_e32 v130, v130
	v_mul_f32_e32 v134, 0xc01d265f, v131
	v_exp_f32_e32 v134, v134
	v_med3_f32 v12, v12, s73, v178
	v_add_f32_e32 v12, 1.0, v12
	v_mul_f32_e32 v17, v17, v130
	v_mul_f32_e32 v17, v12, v17
	v_add_f32_e32 v12, 1.0, v134
	v_rcp_f32_e32 v12, v12
	v_fma_f32 v130, v136, v16, v32
	v_med3_f32 v130, v130, s73, v178
	v_add_f32_e32 v130, 1.0, v130
	v_mul_f32_e32 v12, v131, v12
	v_fma_f32 v131, v140, v16, v24
	v_min_f32_e32 v131, 0x40e00000, v131
	v_mul_f32_e32 v134, 0xc01d265f, v131
	v_exp_f32_e32 v134, v134
	v_mul_f32_e32 v130, v130, v12
	v_fma_f32 v12, v132, v16, v20
	v_med3_f32 v12, v12, s73, v178
	v_add_f32_e32 v132, 1.0, v134
	v_fma_f32 v134, v145, v16, v29
	v_min_f32_e32 v134, 0x40e00000, v134
	v_rcp_f32_e32 v132, v132
	v_mul_f32_e32 v135, 0xc01d265f, v134
	v_exp_f32_e32 v135, v135
	v_add_f32_e32 v12, 1.0, v12
	v_mul_f32_e32 v131, v131, v132
	v_mul_f32_e32 v131, v12, v131
	v_add_f32_e32 v12, 1.0, v135
	v_rcp_f32_e32 v12, v12
	v_fma_f32 v132, v137, v16, v33
	v_med3_f32 v132, v132, s73, v178
	v_add_f32_e32 v132, 1.0, v132
	v_mul_f32_e32 v12, v134, v12
	v_mul_f32_e32 v132, v132, v12
	v_fma_f32 v12, v141, v16, v25
	v_min_f32_e32 v134, 0x40e00000, v12
	v_mul_f32_e32 v12, 0xc01d265f, v134
	v_exp_f32_e32 v12, v12
	v_fma_f32 v16, v133, v16, v21
	v_med3_f32 v16, v16, s73, v178
	v_add_f32_e32 v16, 1.0, v16
	v_add_f32_e32 v12, 1.0, v12
	v_rcp_f32_e32 v133, v12
	v_mov_b32_e32 v12, 0
	v_cvt_pk_fp8_f32 v12, v13, v15
	v_mov_b32_e32 v13, 0
	v_cvt_pk_fp8_f32 v13, v14, v17
	v_mul_f32_e32 v14, v134, v133
	v_mul_f32_e32 v14, v16, v14
	s_waitcnt vmcnt(6)
	v_mul_f32_e32 v16, 0x3c800000, v189
	v_cndmask_b32_e64 v16, 0, v16, s[4:5]
	v_fma_f32 v17, v126, v16, v26
	v_cvt_pk_fp8_f32 v13, v131, v14 op_sel:[0,0,1]
	v_add_u32_e32 v14, s8, v186
	v_min_f32_e32 v17, 0x40e00000, v17
	v_cvt_pk_fp8_f32 v12, v130, v132 op_sel:[0,0,1]
	v_ashrrev_i32_e32 v15, 31, v14
	v_mul_f32_e32 v126, 0xc01d265f, v17
	v_lshlrev_b64 v[14:15], 11, v[14:15]
	v_exp_f32_e32 v126, v126
	v_lshl_add_u64 v[14:15], s[26:27], 0, v[14:15]
	v_lshl_add_u64 v[14:15], v[14:15], 0, v[2:3]
	global_store_dwordx2 v[14:15], v[12:13], off
	v_fma_f32 v14, v122, v16, v22
	v_add_f32_e32 v12, 1.0, v126
	v_min_f32_e32 v14, 0x40e00000, v14
	v_rcp_f32_e32 v12, v12
	v_mul_f32_e32 v15, 0xc01d265f, v14
	v_exp_f32_e32 v15, v15
	v_fma_f32 v13, v118, v16, v30
	v_med3_f32 v13, v13, s73, v178
	v_mul_f32_e32 v12, v17, v12
	v_fma_f32 v17, v127, v16, v27
	v_add_f32_e32 v13, 1.0, v13
	v_add_f32_e32 v15, 1.0, v15
	v_min_f32_e32 v17, 0x40e00000, v17
	v_mul_f32_e32 v13, v13, v12
	v_fma_f32 v12, v114, v16, v18
	v_rcp_f32_e32 v15, v15
	v_mul_f32_e32 v114, 0xc01d265f, v17
	v_exp_f32_e32 v114, v114
	v_med3_f32 v12, v12, s73, v178
	v_add_f32_e32 v12, 1.0, v12
	v_mul_f32_e32 v14, v14, v15
	v_mul_f32_e32 v14, v12, v14
	v_add_f32_e32 v12, 1.0, v114
	v_rcp_f32_e32 v12, v12
	v_fma_f32 v15, v119, v16, v31
	v_med3_f32 v15, v15, s73, v178
	v_add_f32_e32 v15, 1.0, v15
	v_mul_f32_e32 v12, v17, v12
	v_fma_f32 v17, v123, v16, v23
	v_min_f32_e32 v17, 0x40e00000, v17
	v_mul_f32_e32 v114, 0xc01d265f, v17
	v_exp_f32_e32 v114, v114
	v_mul_f32_e32 v15, v15, v12
	v_fma_f32 v12, v115, v16, v19
	v_fma_f32 v115, v128, v16, v28
	v_add_f32_e32 v114, 1.0, v114
	v_min_f32_e32 v115, 0x40e00000, v115
	v_rcp_f32_e32 v114, v114
	v_mul_f32_e32 v118, 0xc01d265f, v115
	v_exp_f32_e32 v118, v118
	v_med3_f32 v12, v12, s73, v178
	v_add_f32_e32 v12, 1.0, v12
	v_mul_f32_e32 v17, v17, v114
	v_mul_f32_e32 v17, v12, v17
	v_add_f32_e32 v12, 1.0, v118
	v_rcp_f32_e32 v12, v12
	v_fma_f32 v114, v120, v16, v32
	v_med3_f32 v114, v114, s73, v178
	v_add_f32_e32 v114, 1.0, v114
	v_mul_f32_e32 v12, v115, v12
	v_fma_f32 v115, v124, v16, v24
	v_min_f32_e32 v115, 0x40e00000, v115
	v_mul_f32_e32 v118, 0xc01d265f, v115
	v_exp_f32_e32 v118, v118
	v_mul_f32_e32 v114, v114, v12
	v_fma_f32 v12, v116, v16, v20
	v_med3_f32 v12, v12, s73, v178
	v_add_f32_e32 v116, 1.0, v118
	v_fma_f32 v118, v129, v16, v29
	v_min_f32_e32 v118, 0x40e00000, v118
	v_rcp_f32_e32 v116, v116
	v_mul_f32_e32 v119, 0xc01d265f, v118
	v_exp_f32_e32 v119, v119
	v_add_f32_e32 v12, 1.0, v12
	v_mul_f32_e32 v115, v115, v116
	v_mul_f32_e32 v115, v12, v115
	v_add_f32_e32 v12, 1.0, v119
	v_rcp_f32_e32 v12, v12
	v_fma_f32 v116, v121, v16, v33
	v_med3_f32 v116, v116, s73, v178
	v_add_f32_e32 v116, 1.0, v116
	v_mul_f32_e32 v12, v118, v12
	v_mul_f32_e32 v116, v116, v12
	v_fma_f32 v12, v125, v16, v25
	v_min_f32_e32 v118, 0x40e00000, v12
	v_mul_f32_e32 v12, 0xc01d265f, v118
	v_exp_f32_e32 v12, v12
	v_fma_f32 v16, v117, v16, v21
	v_med3_f32 v16, v16, s73, v178
	v_add_f32_e32 v16, 1.0, v16
	v_add_f32_e32 v12, 1.0, v12
	v_rcp_f32_e32 v117, v12
	v_mov_b32_e32 v12, 0
	v_cvt_pk_fp8_f32 v12, v13, v15
	v_mov_b32_e32 v13, 0
	v_cvt_pk_fp8_f32 v13, v14, v17
	v_mul_f32_e32 v14, v118, v117
	v_mul_f32_e32 v14, v16, v14
	s_waitcnt vmcnt(6)
; __device__ __forceinline__ unsigned cvt4_fp8(float a, float b, float c, float d) { int w = 0; w = __builtin_amdgcn_cvt_pk_fp8_f32(a, b, w, false); w = __builtin_amdgcn_cvt_pk_fp8_f32(c, d, w, true); return (unsigned)w; }
; __device__ __forceinline__ float sig1702_(float x) { return __builtin_amdgcn_rcpf(1.0f + __builtin_amdgcn_exp2f(x * -2.4554669f)); }
;     __device__ __forceinline__ void operator()(const f32x4 (&acc)[2][2][4][2], const pg8::Unit& u, const Pre& pre, int wr, int wc, int fr, int fq) const {
;     ...
;         for (int i = 0; i < 8; ++i) { const int p = u.r0 + (i >> 2) * 128 + wr * 64 + (i & 3) * 16 + fr; rsv[i] = list_rs[e * LIST_STRIDE + (p < ce ? p : 0)]; }
; #pragma unroll
;         for (int ai = 0; ai < 2; ++ai)
; #pragma unroll
;             for (int m = 0; m < 4; ++m) { const int rit = ai * 128 + wr * 64 + m * 16 + fr, p = u.r0 + rit; const float rs = (p < ce) ? rsv[ai * 4 + m] * 0.015625f : 0.f;
;                 f32x4 gt0 = acc[ai][0][m][0] * rs + g0, gt1 = acc[ai][0][m][1] * rs + g1, up0 = acc[ai][1][m][0] * rs + u0, up1 = acc[ai][1][m][1] * rs + u1;
;                 float o[8];
; #pragma unroll
;                 for (int j = 0; j < 4; ++j) { float gv = fminf(gt0[j], 7.0f), uv = fminf(fmaxf(up0[j], -7.0f), 7.0f); o[j] = (uv + 1.0f) * (gv * sig1702_(gv));
;                     gv = fminf(gt1[j], 7.0f); uv = fminf(fmaxf(up1[j], -7.0f), 7.0f); o[4 + j] = (uv + 1.0f) * (gv * sig1702_(gv)); }
;                 u32x2 w; w.x = cvt4_fp8(o[0], o[1], o[2], o[3]); w.y = cvt4_fp8(o[4], o[5], o[6], o[7]);
;                 *(u32x2*)(ACT + (size_t)(u.pm * 256 + rit) * DFF + col) = w; }
	v_mul_f32_e32 v16, 0x3c800000, v190
	v_cndmask_b32_e64 v16, 0, v16, s[2:3]
	v_fma_f32 v17, v110, v16, v26
	v_cvt_pk_fp8_f32 v13, v115, v14 op_sel:[0,0,1]
	v_add_u32_e32 v14, s8, v187
	v_min_f32_e32 v17, 0x40e00000, v17
	v_cvt_pk_fp8_f32 v12, v114, v116 op_sel:[0,0,1]
	v_ashrrev_i32_e32 v15, 31, v14
	v_mul_f32_e32 v110, 0xc01d265f, v17
	v_lshlrev_b64 v[14:15], 11, v[14:15]
	v_exp_f32_e32 v110, v110
	v_lshl_add_u64 v[14:15], s[26:27], 0, v[14:15]
	v_lshl_add_u64 v[14:15], v[14:15], 0, v[2:3]
	global_store_dwordx2 v[14:15], v[12:13], off
	v_fma_f32 v14, v106, v16, v22
	v_add_f32_e32 v12, 1.0, v110
	v_min_f32_e32 v14, 0x40e00000, v14
	v_rcp_f32_e32 v12, v12
	v_mul_f32_e32 v15, 0xc01d265f, v14
	v_exp_f32_e32 v15, v15
	v_fma_f32 v13, v102, v16, v30
	v_med3_f32 v13, v13, s73, v178
	v_mul_f32_e32 v12, v17, v12
	v_fma_f32 v17, v111, v16, v27
	v_add_f32_e32 v13, 1.0, v13
	v_add_f32_e32 v15, 1.0, v15
	v_min_f32_e32 v17, 0x40e00000, v17
	v_mul_f32_e32 v13, v13, v12
	v_fma_f32 v12, v98, v16, v18
	v_rcp_f32_e32 v15, v15
	v_mul_f32_e32 v98, 0xc01d265f, v17
	v_exp_f32_e32 v98, v98
	v_med3_f32 v12, v12, s73, v178
	v_add_f32_e32 v12, 1.0, v12
	v_mul_f32_e32 v14, v14, v15
	v_mul_f32_e32 v14, v12, v14
	v_add_f32_e32 v12, 1.0, v98
	v_rcp_f32_e32 v12, v12
	v_fma_f32 v15, v103, v16, v31
	v_med3_f32 v15, v15, s73, v178
	v_add_f32_e32 v15, 1.0, v15
	v_mul_f32_e32 v12, v17, v12
	v_fma_f32 v17, v107, v16, v23
	v_min_f32_e32 v17, 0x40e00000, v17
	v_mul_f32_e32 v98, 0xc01d265f, v17
	v_exp_f32_e32 v98, v98
	v_mul_f32_e32 v15, v15, v12
	v_fma_f32 v12, v99, v16, v19
	v_fma_f32 v99, v112, v16, v28
	v_add_f32_e32 v98, 1.0, v98
	v_min_f32_e32 v99, 0x40e00000, v99
	v_rcp_f32_e32 v98, v98
	v_mul_f32_e32 v102, 0xc01d265f, v99
	v_exp_f32_e32 v102, v102
	v_med3_f32 v12, v12, s73, v178
	v_add_f32_e32 v12, 1.0, v12
	v_mul_f32_e32 v17, v17, v98
	v_mul_f32_e32 v17, v12, v17
	v_add_f32_e32 v12, 1.0, v102
	v_rcp_f32_e32 v12, v12
	v_fma_f32 v98, v104, v16, v32
	v_med3_f32 v98, v98, s73, v178
	v_add_f32_e32 v98, 1.0, v98
	v_mul_f32_e32 v12, v99, v12
	v_fma_f32 v99, v108, v16, v24
	v_min_f32_e32 v99, 0x40e00000, v99
	v_mul_f32_e32 v102, 0xc01d265f, v99
	v_exp_f32_e32 v102, v102
	v_mul_f32_e32 v98, v98, v12
	v_fma_f32 v12, v100, v16, v20
	v_med3_f32 v12, v12, s73, v178
	v_add_f32_e32 v100, 1.0, v102
	v_fma_f32 v102, v113, v16, v29
	v_min_f32_e32 v102, 0x40e00000, v102
	v_rcp_f32_e32 v100, v100
	v_mul_f32_e32 v103, 0xc01d265f, v102
	v_exp_f32_e32 v103, v103
	v_add_f32_e32 v12, 1.0, v12
	v_mul_f32_e32 v99, v99, v100
	v_mul_f32_e32 v99, v12, v99
	v_add_f32_e32 v12, 1.0, v103
	v_rcp_f32_e32 v12, v12
	v_fma_f32 v100, v105, v16, v33
	v_med3_f32 v100, v100, s73, v178
	v_add_f32_e32 v100, 1.0, v100
	v_mul_f32_e32 v12, v102, v12
	v_mul_f32_e32 v100, v100, v12
	v_fma_f32 v12, v109, v16, v25
	v_min_f32_e32 v102, 0x40e00000, v12
	v_mul_f32_e32 v12, 0xc01d265f, v102
	v_exp_f32_e32 v12, v12
	v_fma_f32 v16, v101, v16, v21
	v_med3_f32 v16, v16, s73, v178
	v_add_f32_e32 v16, 1.0, v16
	v_add_f32_e32 v12, 1.0, v12
	v_rcp_f32_e32 v101, v12
	v_mov_b32_e32 v12, 0
	v_cvt_pk_fp8_f32 v12, v13, v15
	v_mov_b32_e32 v13, 0
	v_cvt_pk_fp8_f32 v13, v14, v17
	v_mul_f32_e32 v14, v102, v101
	v_mul_f32_e32 v14, v16, v14
	v_cvt_pk_fp8_f32 v12, v98, v100 op_sel:[0,0,1]
	v_cvt_pk_fp8_f32 v13, v99, v14 op_sel:[0,0,1]
	v_add_u32_e32 v14, s8, v10
	s_waitcnt vmcnt(6)
	v_mul_f32_e32 v10, 0x3c800000, v11
	v_cndmask_b32_e32 v16, 0, v10, vcc
	v_fma_f32 v10, v94, v16, v26
	v_ashrrev_i32_e32 v15, 31, v14
	v_min_f32_e32 v17, 0x40e00000, v10
	v_lshlrev_b64 v[14:15], 11, v[14:15]
	v_mul_f32_e32 v10, 0xc01d265f, v17
	v_exp_f32_e32 v94, v10
	v_lshl_add_u64 v[10:11], s[26:27], 0, v[14:15]
	v_lshl_add_u64 v[10:11], v[10:11], 0, v[2:3]
	global_store_dwordx2 v[10:11], v[12:13], off
	v_fma_f32 v12, v90, v16, v22
	v_min_f32_e32 v12, 0x40e00000, v12
	v_mul_f32_e32 v13, 0xc01d265f, v12
	v_exp_f32_e32 v13, v13
	v_add_f32_e32 v10, 1.0, v94
	v_rcp_f32_e32 v10, v10
	v_fma_f32 v14, v95, v16, v27
	v_fma_f32 v11, v86, v16, v30
	v_add_f32_e32 v13, 1.0, v13
	v_min_f32_e32 v14, 0x40e00000, v14
	v_med3_f32 v11, v11, s73, v178
	v_rcp_f32_e32 v13, v13
	v_mul_f32_e32 v15, 0xc01d265f, v14
	v_add_f32_e32 v11, 1.0, v11
	v_mul_f32_e32 v10, v17, v10
	v_exp_f32_e32 v15, v15
	v_mul_f32_e32 v11, v11, v10
	v_fma_f32 v10, v82, v16, v18
	v_med3_f32 v10, v10, s73, v178
	v_add_f32_e32 v10, 1.0, v10
	v_mul_f32_e32 v12, v12, v13
	v_mul_f32_e32 v12, v10, v12
	v_add_f32_e32 v10, 1.0, v15
	v_rcp_f32_e32 v10, v10
	v_fma_f32 v17, v96, v16, v28
	v_fma_f32 v13, v87, v16, v31
	v_min_f32_e32 v17, 0x40e00000, v17
	v_mul_f32_e32 v10, v14, v10
	v_fma_f32 v14, v91, v16, v23
	v_min_f32_e32 v14, 0x40e00000, v14
	v_mul_f32_e32 v15, 0xc01d265f, v14
	v_exp_f32_e32 v15, v15
	v_med3_f32 v13, v13, s73, v178
	v_mul_f32_e32 v82, 0xc01d265f, v17
	v_add_f32_e32 v13, 1.0, v13
	v_add_f32_e32 v15, 1.0, v15
	v_rcp_f32_e32 v15, v15
	v_exp_f32_e32 v82, v82
	v_mul_f32_e32 v13, v13, v10
	v_fma_f32 v10, v83, v16, v19
	v_med3_f32 v10, v10, s73, v178
	v_add_f32_e32 v10, 1.0, v10
	v_mul_f32_e32 v14, v14, v15
	v_mul_f32_e32 v14, v10, v14
	v_add_f32_e32 v10, 1.0, v82
	v_rcp_f32_e32 v10, v10
	v_fma_f32 v15, v88, v16, v32
	v_med3_f32 v15, v15, s73, v178
	v_fma_f32 v83, v97, v16, v29
	v_mul_f32_e32 v10, v17, v10
	v_fma_f32 v17, v92, v16, v24
	v_min_f32_e32 v17, 0x40e00000, v17
	v_mul_f32_e32 v82, 0xc01d265f, v17
	v_exp_f32_e32 v82, v82
	v_add_f32_e32 v15, 1.0, v15
	v_min_f32_e32 v83, 0x40e00000, v83
	v_mul_f32_e32 v15, v15, v10
	v_add_f32_e32 v82, 1.0, v82
	v_fma_f32 v10, v84, v16, v20
	v_rcp_f32_e32 v82, v82
	v_mul_f32_e32 v84, 0xc01d265f, v83
	v_exp_f32_e32 v84, v84
	v_med3_f32 v10, v10, s73, v178
	v_add_f32_e32 v10, 1.0, v10
	v_mul_f32_e32 v17, v17, v82
	v_mul_f32_e32 v17, v10, v17
	v_add_f32_e32 v10, 1.0, v84
	v_rcp_f32_e32 v10, v10
	v_fma_f32 v82, v89, v16, v33
	v_med3_f32 v82, v82, s73, v178
	v_add_f32_e32 v82, 1.0, v82
	v_mul_f32_e32 v10, v83, v10
	v_mul_f32_e32 v82, v82, v10
	v_fma_f32 v10, v93, v16, v25
	v_min_f32_e32 v83, 0x40e00000, v10
	v_mul_f32_e32 v10, 0xc01d265f, v83
	v_exp_f32_e32 v10, v10
	v_fma_f32 v16, v85, v16, v21
	v_med3_f32 v16, v16, s73, v178
	v_add_f32_e32 v16, 1.0, v16
	v_add_f32_e32 v10, 1.0, v10
	v_rcp_f32_e32 v84, v10
	v_mov_b32_e32 v10, 0
	v_cvt_pk_fp8_f32 v10, v11, v13
	v_mov_b32_e32 v11, 0
	v_cvt_pk_fp8_f32 v11, v12, v14
	v_mul_f32_e32 v12, v83, v84
	v_mul_f32_e32 v12, v16, v12
	v_add_u32_e32 v14, 0x90, v5
	v_cvt_pk_fp8_f32 v11, v17, v12 op_sel:[0,0,1]
	v_add_u32_e32 v12, s8, v8
	v_add_u32_e32 v8, s50, v14
	s_waitcnt vmcnt(6)
; __device__ __forceinline__ unsigned cvt4_fp8(float a, float b, float c, float d) { int w = 0; w = __builtin_amdgcn_cvt_pk_fp8_f32(a, b, w, false); w = __builtin_amdgcn_cvt_pk_fp8_f32(c, d, w, true); return (unsigned)w; }
; __device__ __forceinline__ float sig1702_(float x) { return __builtin_amdgcn_rcpf(1.0f + __builtin_amdgcn_exp2f(x * -2.4554669f)); }
;     __device__ __forceinline__ void operator()(const f32x4 (&acc)[2][2][4][2], const pg8::Unit& u, const Pre& pre, int wr, int wc, int fr, int fq) const {
;     ...
;         for (int i = 0; i < 8; ++i) { const int p = u.r0 + (i >> 2) * 128 + wr * 64 + (i & 3) * 16 + fr; rsv[i] = list_rs[e * LIST_STRIDE + (p < ce ? p : 0)]; }
; #pragma unroll
;         for (int ai = 0; ai < 2; ++ai)
; #pragma unroll
;             for (int m = 0; m < 4; ++m) { const int rit = ai * 128 + wr * 64 + m * 16 + fr, p = u.r0 + rit; const float rs = (p < ce) ? rsv[ai * 4 + m] * 0.015625f : 0.f;
;                 f32x4 gt0 = acc[ai][0][m][0] * rs + g0, gt1 = acc[ai][0][m][1] * rs + g1, up0 = acc[ai][1][m][0] * rs + u0, up1 = acc[ai][1][m][1] * rs + u1;
;                 float o[8];
; #pragma unroll
;                 for (int j = 0; j < 4; ++j) { float gv = fminf(gt0[j], 7.0f), uv = fminf(fmaxf(up0[j], -7.0f), 7.0f); o[j] = (uv + 1.0f) * (gv * sig1702_(gv));
;                     gv = fminf(gt1[j], 7.0f); uv = fminf(fmaxf(up1[j], -7.0f), 7.0f); o[4 + j] = (uv + 1.0f) * (gv * sig1702_(gv)); }
;                 u32x2 w; w.x = cvt4_fp8(o[0], o[1], o[2], o[3]); w.y = cvt4_fp8(o[4], o[5], o[6], o[7]);
;                 *(u32x2*)(ACT + (size_t)(u.pm * 256 + rit) * DFF + col) = w; }
	v_mul_f32_e32 v9, 0x3c800000, v9
	v_cmp_lt_i32_e32 vcc, v8, v4
	v_cvt_pk_fp8_f32 v10, v15, v82 op_sel:[0,0,1]
	v_ashrrev_i32_e32 v13, 31, v12
	v_cndmask_b32_e32 v15, 0, v9, vcc
	v_fma_f32 v8, v78, v15, v26
	v_min_f32_e32 v16, 0x40e00000, v8
	v_lshlrev_b64 v[12:13], 11, v[12:13]
	v_mul_f32_e32 v8, 0xc01d265f, v16
	v_exp_f32_e32 v17, v8
	v_lshl_add_u64 v[8:9], s[26:27], 0, v[12:13]
	v_lshl_add_u64 v[8:9], v[8:9], 0, v[2:3]
	global_store_dwordx2 v[8:9], v[10:11], off
	v_fma_f32 v10, v74, v15, v22
	v_min_f32_e32 v10, 0x40e00000, v10
	v_mul_f32_e32 v11, 0xc01d265f, v10
	v_exp_f32_e32 v11, v11
	v_add_f32_e32 v8, 1.0, v17
	v_rcp_f32_e32 v8, v8
	v_fma_f32 v12, v79, v15, v27
	v_fma_f32 v9, v70, v15, v30
	v_add_f32_e32 v11, 1.0, v11
	v_min_f32_e32 v12, 0x40e00000, v12
	v_med3_f32 v9, v9, s73, v178
	v_rcp_f32_e32 v11, v11
	v_mul_f32_e32 v13, 0xc01d265f, v12
	v_add_f32_e32 v9, 1.0, v9
	v_mul_f32_e32 v8, v16, v8
	v_exp_f32_e32 v13, v13
	v_mul_f32_e32 v9, v9, v8
	v_fma_f32 v8, v66, v15, v18
	v_med3_f32 v8, v8, s73, v178
	v_add_f32_e32 v8, 1.0, v8
	v_mul_f32_e32 v10, v10, v11
	v_mul_f32_e32 v10, v8, v10
	v_add_f32_e32 v8, 1.0, v13
	v_rcp_f32_e32 v8, v8
	v_fma_f32 v16, v80, v15, v28
	v_fma_f32 v11, v71, v15, v31
	v_min_f32_e32 v16, 0x40e00000, v16
	v_mul_f32_e32 v8, v12, v8
	v_fma_f32 v12, v75, v15, v23
	v_min_f32_e32 v12, 0x40e00000, v12
	v_mul_f32_e32 v13, 0xc01d265f, v12
	v_exp_f32_e32 v13, v13
	v_med3_f32 v11, v11, s73, v178
	v_mul_f32_e32 v17, 0xc01d265f, v16
	v_add_f32_e32 v11, 1.0, v11
	v_add_f32_e32 v13, 1.0, v13
	v_rcp_f32_e32 v13, v13
	v_exp_f32_e32 v17, v17
	v_mul_f32_e32 v11, v11, v8
	v_fma_f32 v8, v67, v15, v19
	v_med3_f32 v8, v8, s73, v178
	v_add_f32_e32 v8, 1.0, v8
	v_mul_f32_e32 v12, v12, v13
	v_mul_f32_e32 v12, v8, v12
	v_add_f32_e32 v8, 1.0, v17
	v_rcp_f32_e32 v8, v8
	v_fma_f32 v66, v81, v15, v29
	v_fma_f32 v13, v72, v15, v32
	v_min_f32_e32 v66, 0x40e00000, v66
	v_mul_f32_e32 v8, v16, v8
	v_fma_f32 v16, v76, v15, v24
	v_min_f32_e32 v16, 0x40e00000, v16
	v_mul_f32_e32 v17, 0xc01d265f, v16
	v_exp_f32_e32 v17, v17
	v_med3_f32 v13, v13, s73, v178
	v_mul_f32_e32 v67, 0xc01d265f, v66
	v_add_f32_e32 v13, 1.0, v13
	v_add_f32_e32 v17, 1.0, v17
	v_rcp_f32_e32 v17, v17
	v_exp_f32_e32 v67, v67
	v_mul_f32_e32 v13, v13, v8
	v_fma_f32 v8, v68, v15, v20
	v_med3_f32 v8, v8, s73, v178
	v_add_f32_e32 v8, 1.0, v8
	v_mul_f32_e32 v16, v16, v17
	v_mul_f32_e32 v16, v8, v16
	v_add_f32_e32 v8, 1.0, v67
	v_rcp_f32_e32 v8, v8
	v_fma_f32 v17, v73, v15, v33
	v_med3_f32 v17, v17, s73, v178
	v_add_f32_e32 v17, 1.0, v17
	v_mul_f32_e32 v8, v66, v8
	v_mul_f32_e32 v17, v17, v8
	v_fma_f32 v8, v77, v15, v25
	v_min_f32_e32 v66, 0x40e00000, v8
	v_mul_f32_e32 v8, 0xc01d265f, v66
	v_exp_f32_e32 v8, v8
	v_fma_f32 v15, v69, v15, v21
	v_med3_f32 v15, v15, s73, v178
	s_waitcnt vmcnt(6)
	v_mul_f32_e32 v7, 0x3c800000, v7
	v_add_f32_e32 v8, 1.0, v8
	v_rcp_f32_e32 v67, v8
	v_mov_b32_e32 v8, 0
	v_cvt_pk_fp8_f32 v8, v9, v11
	v_mov_b32_e32 v9, 0
	v_cvt_pk_fp8_f32 v9, v10, v12
	v_add_u32_e32 v12, 0xa0, v5
	v_cvt_pk_fp8_f32 v8, v13, v17 op_sel:[0,0,1]
	v_add_u32_e32 v13, s50, v12
	v_cmp_lt_i32_e32 vcc, v13, v4
	v_add_f32_e32 v15, 1.0, v15
	v_mul_f32_e32 v10, v66, v67
	v_cndmask_b32_e32 v7, 0, v7, vcc
	v_mul_f32_e32 v10, v15, v10
	v_fma_f32 v13, v62, v7, v26
	v_cvt_pk_fp8_f32 v9, v16, v10 op_sel:[0,0,1]
	v_add_u32_e32 v10, s8, v14
	v_min_f32_e32 v13, 0x40e00000, v13
	v_ashrrev_i32_e32 v11, 31, v10
	v_mul_f32_e32 v14, 0xc01d265f, v13
	v_lshlrev_b64 v[10:11], 11, v[10:11]
	v_exp_f32_e32 v14, v14
	v_lshl_add_u64 v[10:11], s[26:27], 0, v[10:11]
	v_lshl_add_u64 v[10:11], v[10:11], 0, v[2:3]
	global_store_dwordx2 v[10:11], v[8:9], off
	v_fma_f32 v10, v58, v7, v22
	v_add_f32_e32 v8, 1.0, v14
	v_min_f32_e32 v10, 0x40e00000, v10
	v_rcp_f32_e32 v8, v8
	v_mul_f32_e32 v11, 0xc01d265f, v10
	v_exp_f32_e32 v11, v11
	v_fma_f32 v9, v54, v7, v30
	v_mul_f32_e32 v8, v13, v8
	v_fma_f32 v13, v63, v7, v27
	v_add_f32_e32 v11, 1.0, v11
	v_min_f32_e32 v13, 0x40e00000, v13
	v_med3_f32 v9, v9, s73, v178
	v_rcp_f32_e32 v11, v11
	v_mul_f32_e32 v14, 0xc01d265f, v13
	v_add_f32_e32 v9, 1.0, v9
	v_exp_f32_e32 v14, v14
	v_mul_f32_e32 v9, v9, v8
	v_fma_f32 v8, v50, v7, v18
	v_med3_f32 v8, v8, s73, v178
	v_add_f32_e32 v8, 1.0, v8
	v_mul_f32_e32 v10, v10, v11
	v_mul_f32_e32 v10, v8, v10
	v_add_f32_e32 v8, 1.0, v14
	v_rcp_f32_e32 v8, v8
	v_fma_f32 v15, v64, v7, v28
	v_fma_f32 v11, v55, v7, v31
	v_min_f32_e32 v15, 0x40e00000, v15
	v_mul_f32_e32 v8, v13, v8
	v_fma_f32 v13, v59, v7, v23
	v_min_f32_e32 v13, 0x40e00000, v13
	v_mul_f32_e32 v14, 0xc01d265f, v13
	v_exp_f32_e32 v14, v14
	v_med3_f32 v11, v11, s73, v178
	v_mul_f32_e32 v16, 0xc01d265f, v15
	v_add_f32_e32 v11, 1.0, v11
	v_add_f32_e32 v14, 1.0, v14
	v_rcp_f32_e32 v14, v14
	v_exp_f32_e32 v16, v16
	v_mul_f32_e32 v11, v11, v8
	v_fma_f32 v8, v51, v7, v19
	v_med3_f32 v8, v8, s73, v178
	v_add_f32_e32 v8, 1.0, v8
	v_mul_f32_e32 v13, v13, v14
	v_mul_f32_e32 v13, v8, v13
	v_add_f32_e32 v8, 1.0, v16
	v_rcp_f32_e32 v8, v8
	v_fma_f32 v17, v65, v7, v29
	v_fma_f32 v14, v56, v7, v32
	v_min_f32_e32 v17, 0x40e00000, v17
	v_mul_f32_e32 v8, v15, v8
	v_fma_f32 v15, v60, v7, v24
	v_min_f32_e32 v15, 0x40e00000, v15
	v_mul_f32_e32 v16, 0xc01d265f, v15
	v_exp_f32_e32 v16, v16
	v_med3_f32 v14, v14, s73, v178
	v_mul_f32_e32 v50, 0xc01d265f, v17
	v_add_f32_e32 v14, 1.0, v14
	v_add_f32_e32 v16, 1.0, v16
	v_rcp_f32_e32 v16, v16
	v_exp_f32_e32 v50, v50
	v_mul_f32_e32 v14, v14, v8
	v_fma_f32 v8, v52, v7, v20
	v_med3_f32 v8, v8, s73, v178
	v_add_f32_e32 v8, 1.0, v8
	v_mul_f32_e32 v15, v15, v16
	v_mul_f32_e32 v15, v8, v15
	v_add_f32_e32 v8, 1.0, v50
	v_rcp_f32_e32 v8, v8
	v_fma_f32 v16, v57, v7, v33
	v_med3_f32 v16, v16, s73, v178
	v_add_f32_e32 v16, 1.0, v16
	v_mul_f32_e32 v8, v17, v8
	v_mul_f32_e32 v16, v16, v8
	v_fma_f32 v8, v61, v7, v25
	v_min_f32_e32 v17, 0x40e00000, v8
	v_mul_f32_e32 v8, 0xc01d265f, v17
	v_exp_f32_e32 v8, v8
	v_fma_f32 v7, v53, v7, v21
	v_med3_f32 v7, v7, s73, v178
	v_add_f32_e32 v7, 1.0, v7
	v_add_f32_e32 v8, 1.0, v8
	v_rcp_f32_e32 v50, v8
	v_mov_b32_e32 v8, 0
	v_cvt_pk_fp8_f32 v8, v9, v11
	v_mov_b32_e32 v9, 0
	v_cvt_pk_fp8_f32 v9, v10, v13
	v_mul_f32_e32 v10, v17, v50
	v_mul_f32_e32 v7, v7, v10
	s_waitcnt vmcnt(6)
; __device__ __forceinline__ unsigned cvt4_fp8(float a, float b, float c, float d) { int w = 0; w = __builtin_amdgcn_cvt_pk_fp8_f32(a, b, w, false); w = __builtin_amdgcn_cvt_pk_fp8_f32(c, d, w, true); return (unsigned)w; }
; __device__ __forceinline__ float sig1702_(float x) { return __builtin_amdgcn_rcpf(1.0f + __builtin_amdgcn_exp2f(x * -2.4554669f)); }
; #define PG8_BAR __builtin_amdgcn_s_barrier()
; template <class Epi, class Sched, bool GATHER, bool ALIGN_EPI, bool SP2, bool FP8>
; __device__ __forceinline__ void gemm_phase(LAS unsigned char* lds, const Gemm g, const Sched& S, const Epi& E) {
;     ...
;         if constexpr (ALIGN_EPI) { if (wr == 0) PG8_BAR; }
;     __device__ __forceinline__ void operator()(const f32x4 (&acc)[2][2][4][2], const pg8::Unit& u, const Pre& pre, int wr, int wc, int fr, int fq) const {
;     ...
;             for (int m = 0; m < 4; ++m) { const int rit = ai * 128 + wr * 64 + m * 16 + fr, p = u.r0 + rit; const float rs = (p < ce) ? rsv[ai * 4 + m] * 0.015625f : 0.f;
;                 f32x4 gt0 = acc[ai][0][m][0] * rs + g0, gt1 = acc[ai][0][m][1] * rs + g1, up0 = acc[ai][1][m][0] * rs + u0, up1 = acc[ai][1][m][1] * rs + u1;
;                 float o[8];
; #pragma unroll
;                 for (int j = 0; j < 4; ++j) { float gv = fminf(gt0[j], 7.0f), uv = fminf(fmaxf(up0[j], -7.0f), 7.0f); o[j] = (uv + 1.0f) * (gv * sig1702_(gv));
;                     gv = fminf(gt1[j], 7.0f); uv = fminf(fmaxf(up1[j], -7.0f), 7.0f); o[4 + j] = (uv + 1.0f) * (gv * sig1702_(gv)); }
;                 u32x2 w; w.x = cvt4_fp8(o[0], o[1], o[2], o[3]); w.y = cvt4_fp8(o[4], o[5], o[6], o[7]);
;                 *(u32x2*)(ACT + (size_t)(u.pm * 256 + rit) * DFF + col) = w; }
	v_mul_f32_e32 v6, 0x3c800000, v6
	v_cvt_pk_fp8_f32 v9, v15, v7 op_sel:[0,0,1]
	v_add_u32_e32 v7, 0xb0, v5
	v_add_u32_e32 v5, s50, v7
	v_cmp_lt_i32_e32 vcc, v5, v4
	v_add_u32_e32 v10, s8, v12
	v_cvt_pk_fp8_f32 v8, v14, v16 op_sel:[0,0,1]
	v_cndmask_b32_e32 v6, 0, v6, vcc
	v_fma_f32 v4, v46, v6, v26
	v_ashrrev_i32_e32 v11, 31, v10
	v_min_f32_e32 v12, 0x40e00000, v4
	v_lshlrev_b64 v[10:11], 11, v[10:11]
	v_mul_f32_e32 v4, 0xc01d265f, v12
	v_exp_f32_e32 v13, v4
	v_lshl_add_u64 v[4:5], s[26:27], 0, v[10:11]
	v_lshl_add_u64 v[4:5], v[4:5], 0, v[2:3]
	global_store_dwordx2 v[4:5], v[8:9], off
	v_fma_f32 v8, v42, v6, v22
	v_min_f32_e32 v8, 0x40e00000, v8
	v_mul_f32_e32 v9, 0xc01d265f, v8
	v_exp_f32_e32 v9, v9
	v_add_f32_e32 v4, 1.0, v13
	v_rcp_f32_e32 v4, v4
	v_fma_f32 v10, v47, v6, v27
	v_fma_f32 v5, v38, v6, v30
	v_add_f32_e32 v9, 1.0, v9
	v_min_f32_e32 v10, 0x40e00000, v10
	v_med3_f32 v5, v5, s73, v178
	v_rcp_f32_e32 v9, v9
	v_mul_f32_e32 v11, 0xc01d265f, v10
	v_add_f32_e32 v5, 1.0, v5
	v_mul_f32_e32 v4, v12, v4
	v_exp_f32_e32 v11, v11
	v_mul_f32_e32 v5, v5, v4
	v_fma_f32 v4, v34, v6, v18
	v_med3_f32 v4, v4, s73, v178
	v_add_f32_e32 v4, 1.0, v4
	v_mul_f32_e32 v8, v8, v9
	v_mul_f32_e32 v8, v4, v8
	v_add_f32_e32 v4, 1.0, v11
	v_rcp_f32_e32 v4, v4
	v_fma_f32 v12, v48, v6, v28
	v_fma_f32 v9, v39, v6, v31
	v_min_f32_e32 v12, 0x40e00000, v12
	v_mul_f32_e32 v4, v10, v4
	v_fma_f32 v10, v43, v6, v23
	v_min_f32_e32 v10, 0x40e00000, v10
	v_mul_f32_e32 v11, 0xc01d265f, v10
	v_exp_f32_e32 v11, v11
	v_med3_f32 v9, v9, s73, v178
	v_mul_f32_e32 v13, 0xc01d265f, v12
	v_add_f32_e32 v9, 1.0, v9
	v_add_f32_e32 v11, 1.0, v11
	v_rcp_f32_e32 v11, v11
	v_exp_f32_e32 v13, v13
	v_mul_f32_e32 v9, v9, v4
	v_fma_f32 v4, v35, v6, v19
	v_med3_f32 v4, v4, s73, v178
	v_add_f32_e32 v4, 1.0, v4
	v_mul_f32_e32 v10, v10, v11
	v_mul_f32_e32 v10, v4, v10
	v_add_f32_e32 v4, 1.0, v13
	v_rcp_f32_e32 v4, v4
	v_fma_f32 v14, v49, v6, v29
	v_fma_f32 v11, v40, v6, v32
	v_min_f32_e32 v14, 0x40e00000, v14
	v_mul_f32_e32 v4, v12, v4
	v_fma_f32 v12, v44, v6, v24
	v_min_f32_e32 v12, 0x40e00000, v12
	v_mul_f32_e32 v13, 0xc01d265f, v12
	v_exp_f32_e32 v13, v13
	v_med3_f32 v11, v11, s73, v178
	v_mul_f32_e32 v15, 0xc01d265f, v14
	v_add_f32_e32 v11, 1.0, v11
	v_add_f32_e32 v13, 1.0, v13
	v_rcp_f32_e32 v13, v13
	v_exp_f32_e32 v15, v15
	v_mul_f32_e32 v11, v11, v4
	v_fma_f32 v4, v36, v6, v20
	v_med3_f32 v4, v4, s73, v178
	v_add_f32_e32 v4, 1.0, v4
	v_mul_f32_e32 v12, v12, v13
	v_mul_f32_e32 v12, v4, v12
	v_add_f32_e32 v4, 1.0, v15
	v_rcp_f32_e32 v4, v4
	v_fma_f32 v13, v41, v6, v33
	v_med3_f32 v13, v13, s73, v178
	v_add_f32_e32 v13, 1.0, v13
	v_mul_f32_e32 v4, v14, v4
	v_mul_f32_e32 v13, v13, v4
	v_fma_f32 v4, v45, v6, v25
	v_min_f32_e32 v14, 0x40e00000, v4
	v_mul_f32_e32 v4, 0xc01d265f, v14
	v_exp_f32_e32 v4, v4
	v_fma_f32 v6, v37, v6, v21
	v_med3_f32 v6, v6, s73, v178
	v_add_f32_e32 v6, 1.0, v6
	v_add_f32_e32 v4, 1.0, v4
	v_rcp_f32_e32 v15, v4
	v_mov_b32_e32 v4, 0
	v_cvt_pk_fp8_f32 v4, v5, v9
	v_mov_b32_e32 v5, 0
	v_cvt_pk_fp8_f32 v5, v8, v10
	v_mul_f32_e32 v8, v14, v15
	v_mul_f32_e32 v6, v6, v8
	v_cvt_pk_fp8_f32 v4, v11, v13 op_sel:[0,0,1]
	v_cvt_pk_fp8_f32 v5, v12, v6 op_sel:[0,0,1]
	v_add_u32_e32 v6, s8, v7
	v_ashrrev_i32_e32 v7, 31, v6
	v_lshlrev_b64 v[6:7], 11, v[6:7]
	v_lshl_add_u64 v[6:7], s[26:27], 0, v[6:7]
	v_lshl_add_u64 v[2:3], v[6:7], 0, v[2:3]
	s_and_b64 vcc, exec, s[30:31]
	s_cbranch_vccz .Lhyb_p5
	s_barrier
.Lhyb_p5:
	s_and_b64 vcc, exec, s[0:1]
	s_mov_b64 s[0:1], -1
	global_store_dwordx2 v[2:3], v[4:5], off
	s_cbranch_vccnz .LBB0_925
	s_andn2_b64 vcc, exec, s[54:55]
	s_cbranch_vccnz .LBB0_924
	s_barrier
	s_branch .LBB0_924
